# v40 plus static s_setprio 3 for the recurrent wave (its polls/LDS ops win CU arbitration over projector and publisher waves)
# speedup vs baseline: 1.0172x; 1.0096x over previous
.LBB0_33:
	s_andn2_saveexec_b64 s[24:25], s[24:25]
	s_cbranch_execz .LBB0_67
	s_setprio 3
	s_lshl_b32 s4, s3, 5
	s_add_i32 s4, s4, s33
	s_ashr_i32 s5, s4, 31
	s_lshl_b64 s[4:5], s[4:5], 14
	s_add_u32 s4, s42, s4
	s_addc_u32 s5, s43, s5
	v_mov_b32_e32 v107, 0
	v_lshlrev_b32_e32 v106, 4, v130
	v_lshl_add_u64 v[42:43], s[4:5], 0, v[106:107]
	s_movk_i32 s6, 0x1000
	v_add_co_u32_e32 v66, vcc, s6, v42
	s_movk_i32 s6, 0x2000
	s_nop 0
	v_addc_co_u32_e32 v67, vcc, 0, v43, vcc
	v_add_co_u32_e32 v44, vcc, s6, v42
	global_load_dwordx4 v[2:5], v106, s[4:5] offset:1024
	global_load_dwordx4 v[6:9], v106, s[4:5] offset:2048
	v_addc_co_u32_e32 v45, vcc, 0, v43, vcc
	global_load_dwordx4 v[10:13], v106, s[4:5] offset:3072
	global_load_dwordx4 v[14:17], v[44:45], off offset:-4096
	global_load_dwordx4 v[18:21], v[66:67], off offset:1024
	global_load_dwordx4 v[22:25], v[66:67], off offset:2048
	global_load_dwordx4 v[26:29], v[44:45], off
	global_load_dwordx4 v[30:33], v[44:45], off offset:1024
	global_load_dwordx4 v[34:37], v[44:45], off offset:2048
	global_load_dwordx4 v[38:41], v[44:45], off offset:3072
	s_movk_i32 s6, 0x3000
	v_add_co_u32_e32 v68, vcc, s6, v42
	s_mul_i32 s26, s3, 0x3c000
	s_nop 0
	v_addc_co_u32_e32 v69, vcc, 0, v43, vcc
	global_load_dwordx4 v[42:45], v[66:67], off offset:3072
	global_load_dwordx4 v[46:49], v[68:69], off
	global_load_dwordx4 v[50:53], v[68:69], off offset:1024
	global_load_dwordx4 v[54:57], v[68:69], off offset:2048
	global_load_dwordx4 v[58:61], v106, s[4:5]
	global_load_dwordx4 v[62:65], v[68:69], off offset:3072
	s_add_u32 s34, s8, s26
	s_addc_u32 s35, s9, 0
	s_add_u32 s36, s34, 0xf0000
	s_addc_u32 s37, s35, 0
	s_cmp_eq_u32 s3, 0
	s_cselect_b64 s[26:27], -1, 0
	s_and_b64 s[28:29], s[26:27], exec
	v_lshrrev_b32_e32 v1, 2, v0
	s_cselect_b32 s44, -1, 1
	s_lshl_b32 s28, s33, 7
	v_mov_b32_e32 v66, 0xc0b8aa3b
	v_cmp_lt_u32_e64 s[6:7], 31, v130
	v_and_b32_e32 v98, 4, v1
	v_mov_b32_e32 v1, 0x4038aa3b
	s_ashr_i32 s29, s28, 31
	v_cndmask_b32_e64 v100, v66, 1.0, s[6:7]
	v_cndmask_b32_e64 v102, v1, 0, s[6:7]
	v_add_u32_e32 v1, 0, v106
	v_lshlrev_b32_e32 v66, 3, v130
	s_lshl_b64 s[28:29], s[28:29], 1
	v_sub_u32_e32 v99, v1, v66
	s_add_u32 s38, s34, s28
	v_lshlrev_b32_e32 v66, 4, v0
	s_addc_u32 s39, s35, s29
	v_and_b32_e32 v106, 0xf0, v66
	v_lshl_add_u64 v[66:67], s[38:39], 0, v[106:107]
	v_lshlrev_b32_e32 v106, 1, v98
	v_cmp_gt_u32_e64 s[4:5], 32, v130
	s_mov_b32 s31, 0
	v_lshlrev_b32_e32 v104, 3, v0
	v_lshl_add_u64 v[108:109], v[66:67], 0, v[106:107]
	v_mov_b32_e32 v103, v102
	v_mov_b32_e32 v101, v100
	s_mov_b64 s[38:39], 0x1000
	s_mov_b32 s45, 0xfffeffff
	s_mov_b32 s46, 0
	v_mov_b32_e32 v110, 0
	v_mov_b32_e32 v111, v107
	v_mov_b32_e32 v112, 0
	v_mov_b32_e32 v113, v107
	s_waitcnt vmcnt(0)
	s_mov_b32 s54, 0
	s_mov_b32 s59, 0xfffeffff
	s_mul_i32 s56, s44, 0xffffe000
	s_ashr_i32 s57, s56, 31
	s_cmp_eq_u32 s3, 0
	s_cselect_b32 s58, 0, 29
	s_lshl_b32 s60, s58, 13
	s_sub_u32 s60, s60, s56
	s_subb_u32 s61, 0, s57
	v_lshlrev_b32_e32 v196, 4, v130
	v_mov_b32_e32 v197, 0
	v_lshl_add_u64 v[196:197], v[196:197], 0, s[60:61]
	v_lshl_add_u64 v[200:201], s[36:37], 0, v[196:197]
	v_lshl_add_u64 v[196:197], s[34:35], 0, v[196:197]
	v_lshl_add_u64 v[198:199], v[196:197], 0, s[38:39]
	v_lshl_add_u64 v[202:203], v[200:201], 0, s[38:39]
